# 128-byte touch spacing + conversion blocks issue their loads before the warm chain
# baseline (speedup 1.0000x reference)
_Z7k_frontPKiS0_PiS1_PjPKfS4_S4_P15HIP_vector_typeIjLj4EES7_PKS5_IfLj4EES7_S7_:
	s_load_dword s36, s[0:1], 0x0
	s_load_dword s37, s[0:1], 0x40
	v_lshrrev_b32_e32 v1, 6, v0
	s_nop 0
	v_readfirstlane_b32 s35, v1
	s_cmpk_lt_u32 s2, 207
	s_cbranch_scc1 .Lmy_cvt0_preskip
	s_waitcnt lgkmcnt(0)
	s_load_dwordx4 s[20:23], s[0:1], 0x50
	s_sub_i32 s3, s2, 207
	v_and_b32_e32 v1, 0x3c0, v0
	v_and_b32_e32 v2, 63, v0
	v_lshlrev_b32_e32 v3, 5, v1
	v_lshl_or_b32 v3, v2, 4, v3
	v_and_b32_e32 v4, 1, v0
	v_lshrrev_b32_e32 v5, 1, v2
	v_lshl_or_b32 v5, v4, 5, v5
	v_add_u32_e32 v5, v5, v1
	v_lshlrev_b32_e32 v5, 4, v5
	v_cmp_eq_u32_e32 vcc, 0, v4
	s_waitcnt lgkmcnt(0)
	s_add_i32 s8, s3, 0
	s_lshl_b32 s9, s8, 10
	s_sub_i32 s9, 0x1869c0, s9
	v_cmp_ge_i32_e64 s[24:25], s9, v1
	s_add_i32 s8, s3, 0
	s_lshl_b32 s9, s8, 15
	s_add_u32 s10, s20, s9
	s_addc_u32 s11, s21, 0
	s_mov_b64 exec, s[24:25]
	global_load_dwordx4 v[8:11], v3, s[10:11] nt
	global_load_dwordx4 v[12:15], v3, s[10:11] offset:1024 nt
	s_mov_b64 exec, -1
.Lmy_cvt0_preskip:
	s_movk_i32 s34, 0x5aa5
	s_mov_b64 exec, 0
	s_cmpk_lt_u32 s35, 8
	s_cbranch_scc1 .Lw0s0d0_16
	s_cmpk_lt_u32 s35, 12
	s_cbranch_scc1 .Lw0s0d8_16
	s_cmpk_lt_u32 s35, 14
	s_cbranch_scc1 .Lw0s0d12_16
	s_cmpk_lt_u32 s35, 15
	s_cbranch_scc1 .Lw0s0d14_16
	s_branch .Lw0t15

.Lmy_cvt0:
	v_cmp_eq_u32_e32 vcc, 0, v4
	s_waitcnt vmcnt(0)
	s_add_i32 s8, s3, 0
	s_lshl_b32 s9, s8, 14
	s_add_u32 s10, s22, s9
	s_addc_u32 s11, s23, 0
	s_mov_b64 exec, s[24:25]
	v_cvt_pk_f16_f32 v8, v8, v9
	v_cvt_pk_f16_f32 v9, v10, v11
	v_cvt_pk_f16_f32 v10, v12, v13
	v_cvt_pk_f16_f32 v11, v14, v15

.Lw0b34:
	v_cndmask_b32_e32 v12, v8, v10, vcc
	v_cndmask_b32_e32 v13, v9, v11, vcc
	s_nop 1
	v_mov_b32_dpp v12, v12 quad_perm:[1,0,3,2] row_mask:0xf bank_mask:0xf bound_ctrl:1
	v_mov_b32_dpp v13, v13 quad_perm:[1,0,3,2] row_mask:0xf bank_mask:0xf bound_ctrl:1
	v_cndmask_b32_e32 v8, v12, v8, vcc
	v_cndmask_b32_e32 v9, v13, v9, vcc
	v_cndmask_b32_e32 v10, v10, v12, vcc
	v_cndmask_b32_e32 v11, v11, v13, vcc
	global_store_dwordx4 v5, v[8:11], s[10:11] sc1

_Z8k_bucketPKiS0_PKjPiS3_PK15HIP_vector_typeIfLj4EEPS4_IjLj4EE:
	s_load_dword s66, s[0:1], 0x0
	s_load_dword s67, s[0:1], 0x40
	v_lshrrev_b32_e32 v1, 6, v0
	s_nop 0
	v_readfirstlane_b32 s65, v1
	s_cmpk_lt_u32 s2, 392
	s_cbranch_scc1 .Lmy_cvt1_preskip
	s_waitcnt lgkmcnt(0)
	s_load_dwordx4 s[20:23], s[0:1], 0x28
	s_sub_i32 s3, s2, 392
	s_cmp_ge_u32 s3, 193
	s_cbranch_scc1 .Lmy_cvt1_end
	v_and_b32_e32 v1, 0x3c0, v0
	v_and_b32_e32 v2, 63, v0
	v_lshlrev_b32_e32 v3, 5, v1
	v_lshl_or_b32 v3, v2, 4, v3
	v_and_b32_e32 v4, 1, v0
	v_lshrrev_b32_e32 v5, 1, v2
	v_lshl_or_b32 v5, v4, 5, v5
	v_add_u32_e32 v5, v5, v1
	v_lshlrev_b32_e32 v5, 4, v5
	v_cmp_eq_u32_e32 vcc, 0, v4
	s_waitcnt lgkmcnt(0)
	s_add_i32 s8, s3, 792
	s_lshl_b32 s9, s8, 10
	s_sub_i32 s9, 0x1869c0, s9
	v_cmp_ge_i32_e64 s[24:25], s9, v1
	s_add_i32 s8, s3, 985
	s_lshl_b32 s9, s8, 10
	s_sub_i32 s9, 0x1869c0, s9
	v_cmp_ge_i32_e64 s[26:27], s9, v1
	s_add_i32 s8, s3, 1178
	s_lshl_b32 s9, s8, 10
	s_sub_i32 s9, 0x1869c0, s9
	v_cmp_ge_i32_e64 s[28:29], s9, v1
	s_add_i32 s8, s3, 1371
	s_lshl_b32 s9, s8, 10
	s_sub_i32 s9, 0x1869c0, s9
	v_cmp_ge_i32_e64 s[30:31], s9, v1
	s_add_i32 s8, s3, 792
	s_lshl_b32 s9, s8, 15
	s_add_u32 s10, s20, s9
	s_addc_u32 s11, s21, 0
	s_mov_b64 exec, s[24:25]
	global_load_dwordx4 v[8:11], v3, s[10:11] nt
	global_load_dwordx4 v[12:15], v3, s[10:11] offset:1024 nt
	s_add_i32 s8, s3, 985
	s_lshl_b32 s9, s8, 15
	s_add_u32 s10, s20, s9
	s_addc_u32 s11, s21, 0
	s_mov_b64 exec, s[26:27]
	global_load_dwordx4 v[16:19], v3, s[10:11] nt
	global_load_dwordx4 v[20:23], v3, s[10:11] offset:1024 nt
	s_add_i32 s8, s3, 1178
	s_lshl_b32 s9, s8, 15
	s_add_u32 s10, s20, s9
	s_addc_u32 s11, s21, 0
	s_mov_b64 exec, s[28:29]
	global_load_dwordx4 v[24:27], v3, s[10:11] nt
	global_load_dwordx4 v[28:31], v3, s[10:11] offset:1024 nt
	s_add_i32 s8, s3, 1371
	s_lshl_b32 s9, s8, 15
	s_add_u32 s10, s20, s9
	s_addc_u32 s11, s21, 0
	s_mov_b64 exec, s[30:31]
	global_load_dwordx4 v[32:35], v3, s[10:11] nt
	global_load_dwordx4 v[36:39], v3, s[10:11] offset:1024 nt
	s_mov_b64 exec, -1
.Lmy_cvt1_preskip:
	s_movk_i32 s64, 0x5aa5
	s_mov_b64 exec, 0
	s_cmpk_lt_u32 s65, 8
	s_cbranch_scc1 .Lw1s0d0_16
	s_cmpk_lt_u32 s65, 12
	s_cbranch_scc1 .Lw1s0d8_16
	s_cmpk_lt_u32 s65, 14
	s_cbranch_scc1 .Lw1s0d12_16
	s_cmpk_lt_u32 s65, 15
	s_cbranch_scc1 .Lw1s0d14_16
	s_branch .Lw1t15

.Lw1b0:
	v_mov_b32_e32 v1, 0xc4
	v_sub_co_u32_e32 v1, vcc, s2, v1
	s_and_b64 s[4:5], vcc, exec
	v_readfirstlane_b32 s3, v1
	s_cselect_b32 s33, s2, s3
	s_cmpk_gt_u32 s2, 0xc3
	s_cselect_b64 s[30:31], -1, 0
	s_and_b64 s[4:5], s[30:31], exec
	s_cselect_b32 s3, 0xc4, 0
	s_add_i32 s3, s3, s33
	s_movk_i32 s6, 0x62
	s_mul_hi_u32 s5, s3, 0x62
	s_mul_i32 s4, s3, 0x62
	v_cmp_gt_u32_e32 vcc, s6, v0
	v_mov_b32_e32 v1, 0
	v_mov_b32_e32 v2, 0
	s_and_saveexec_b64 s[6:7], vcc
	s_cbranch_execz .LBB1_3
	s_load_dwordx2 s[8:9], s[0:1], 0x0

.Lw1b1:
	s_lshl_b64 s[10:11], s[4:5], 2
	v_lshlrev_b32_e32 v2, 2, v0
	s_waitcnt lgkmcnt(0)
	s_add_u32 s8, s8, s10
	s_addc_u32 s9, s9, s11
	global_load_dword v2, v2, s[8:9]

.LBB1_5:
	s_or_b64 exec, exec, s[6:7]
	v_add_u32_dpp v3, v3, v3 row_shr:1 row_mask:0xf bank_mask:0xf bound_ctrl:1
	v_and_b32_e32 v5, 63, v0
	v_cmp_eq_u32_e64 s[4:5], 63, v5
.Lw1t2:
	s_cbranch_execz .Lw1c2
.Lw1b2:
	v_add_u32_dpp v3, v3, v3 row_shr:2 row_mask:0xf bank_mask:0xf bound_ctrl:1
	s_nop 1
	v_add_u32_dpp v3, v3, v3 row_shr:4 row_mask:0xf bank_mask:0xf bound_ctrl:1
	s_nop 1
	v_add_u32_dpp v4, v3, v3 row_shr:8 row_mask:0xf bank_mask:0xf bound_ctrl:1
	s_waitcnt vmcnt(0)
	v_add_u32_dpp v3, v2, v2 row_shr:1 row_mask:0xf bank_mask:0xf bound_ctrl:1
	v_add_u32_dpp v4, v4, v4 row_bcast:15 row_mask:0xa bank_mask:0xf
	s_nop 0
	v_add_u32_dpp v3, v3, v3 row_shr:2 row_mask:0xf bank_mask:0xf bound_ctrl:1
	v_mov_b32_dpp v1, v4 row_bcast:31 row_mask:0xc bank_mask:0xf
	s_nop 0
	v_add_u32_dpp v3, v3, v3 row_shr:4 row_mask:0xf bank_mask:0xf bound_ctrl:1
	s_nop 1
	v_add_u32_dpp v3, v3, v3 row_shr:8 row_mask:0xf bank_mask:0xf bound_ctrl:1
	s_nop 1
	v_add_u32_dpp v3, v3, v3 row_bcast:15 row_mask:0xa bank_mask:0xf
	s_nop 1
	v_add_u32_dpp v3, v3, v3 row_bcast:31 row_mask:0xc bank_mask:0xf

.Lw1b3:
	s_and_saveexec_b64 s[6:7], s[4:5]
	s_cbranch_execz .LBB1_7
	v_lshrrev_b32_e32 v5, 4, v0
	v_and_b32_e32 v5, 60, v5
	v_add_u32_e32 v6, 0x11b20, v5
	v_add_u32_e32 v5, 0x11b60, v5
	v_add_u32_e32 v1, v4, v1
	ds_write_b32 v5, v3
	ds_write_b32 v6, v1

.LBB1_9:
	s_or_b64 exec, exec, s[6:7]
	v_mov_b32_e32 v1, 0x11b20
.Lw1t4:
	s_cbranch_execz .Lw1c4
.Lw1b4:
	s_waitcnt lgkmcnt(0)
	s_barrier
	ds_read_b128 v[4:7], v1
	v_mov_b32_e32 v1, 0x11b30
	ds_read_b128 v[8:11], v1
	v_mov_b32_e32 v1, 0x11b40
	s_movk_i32 s3, 0x7f
	s_waitcnt lgkmcnt(1)
	v_readfirstlane_b32 s40, v4
	v_readfirstlane_b32 s41, v5
	v_readfirstlane_b32 s42, v6
	v_readfirstlane_b32 s43, v7
	ds_read_b128 v[4:7], v1
	v_mov_b32_e32 v1, 0x11b50
	s_waitcnt lgkmcnt(1)
	v_readfirstlane_b32 s44, v8
	v_readfirstlane_b32 s45, v9
	v_readfirstlane_b32 s46, v10
	v_readfirstlane_b32 s47, v11
	ds_read_b128 v[8:11], v1
	v_mov_b32_e32 v1, 0x11b60
	s_waitcnt lgkmcnt(1)

.Lw1b5:
	v_readfirstlane_b32 s48, v4
	v_readfirstlane_b32 s49, v5
	v_readfirstlane_b32 s50, v6
	v_readfirstlane_b32 s51, v7
	s_waitcnt lgkmcnt(0)
	v_readfirstlane_b32 s52, v8
	ds_read_b128 v[4:7], v1
	v_mov_b32_e32 v8, 0x11b70
	v_readfirstlane_b32 s53, v9
	v_readfirstlane_b32 s54, v10
	v_readfirstlane_b32 s55, v11
	ds_read_b128 v[8:11], v8
	v_cmp_lt_u32_e64 s[8:9], s3, v0
	s_movk_i32 s3, 0xbf
	v_cmp_lt_u32_e64 s[10:11], s3, v0
	s_movk_i32 s3, 0xff
	v_cmp_lt_u32_e64 s[12:13], s3, v0
	s_movk_i32 s3, 0x13f
	v_cmp_gt_u32_e64 s[6:7], 64, v0
	v_cmp_lt_u32_e64 s[14:15], s3, v0
	s_movk_i32 s3, 0x17f
	s_waitcnt lgkmcnt(1)
	v_cndmask_b32_e64 v4, v4, 0, s[6:7]

.Lw1b6:
	v_cndmask_b32_e64 v5, 0, v5, s[8:9]
	v_cndmask_b32_e64 v6, 0, v6, s[10:11]
	v_cmp_lt_u32_e64 s[16:17], s3, v0
	s_movk_i32 s3, 0x1bf
	v_add3_u32 v4, v5, v4, v6
	v_cndmask_b32_e64 v5, 0, v7, s[12:13]
	s_waitcnt lgkmcnt(0)
	v_cndmask_b32_e64 v6, 0, v8, s[14:15]
	v_cmp_lt_u32_e64 s[18:19], s3, v0
	v_add3_u32 v4, v5, v4, v6
	v_cndmask_b32_e64 v5, 0, v9, s[16:17]
	v_cndmask_b32_e64 v6, 0, v10, s[18:19]
	v_add3_u32 v12, v5, v4, v6
	v_mov_b32_e32 v4, 0x11b80
	ds_read_b128 v[4:7], v4
	s_movk_i32 s3, 0x1ff
	v_cmp_lt_u32_e64 s[20:21], s3, v0

.Lw1b7:
	s_movk_i32 s3, 0x23f
	v_mov_b32_e32 v8, 0x11b90
	v_cndmask_b32_e64 v11, 0, v11, s[20:21]
	ds_read_b96 v[8:10], v8
	v_cmp_lt_u32_e64 s[20:21], s3, v0
	s_movk_i32 s3, 0x27f
	s_load_dwordx2 s[24:25], s[0:1], 0x10
	s_waitcnt lgkmcnt(0)
	v_cndmask_b32_e64 v4, 0, v4, s[20:21]
	v_cmp_lt_u32_e64 s[20:21], s3, v0
	s_movk_i32 s3, 0x2bf
	v_add3_u32 v4, v11, v12, v4
	v_cndmask_b32_e64 v5, 0, v5, s[20:21]
	v_cmp_lt_u32_e64 s[20:21], s3, v0
	s_movk_i32 s3, 0x2ff
	v_lshrrev_b32_e32 v1, 6, v0
	v_cndmask_b32_e64 v6, 0, v6, s[20:21]
	v_cmp_lt_u32_e64 s[20:21], s3, v0

.Lw1b8:
	s_movk_i32 s3, 0x33f
	v_add3_u32 v4, v5, v4, v6
	v_cndmask_b32_e64 v5, 0, v7, s[20:21]
	v_cmp_lt_u32_e64 s[20:21], s3, v0
	s_movk_i32 s3, 0x37f
	s_nop 0
	v_cndmask_b32_e64 v6, 0, v8, s[20:21]
	v_cmp_lt_u32_e64 s[20:21], s3, v0
	v_add3_u32 v4, v5, v4, v6
	s_nop 0
	v_cndmask_b32_e64 v5, 0, v9, s[20:21]
	v_cmp_eq_u32_e64 s[20:21], 15, v1
	s_nop 1
	v_cndmask_b32_e64 v6, 0, v10, s[20:21]
	v_add3_u32 v4, v5, v4, v6
	s_and_saveexec_b64 s[26:27], vcc
	v_mov_b32_e32 v5, 0x11800
	v_sub_u32_e32 v2, v3, v2
	v_lshl_add_u32 v5, v0, 2, v5

.Lw1b9:
	v_add_u32_e32 v2, v2, v4
	ds_write_b32 v5, v2
	s_or_b64 exec, exec, s[26:27]
	s_movk_i32 s3, 0x61
	v_cmp_eq_u32_e32 vcc, s3, v0
	s_and_saveexec_b64 s[26:27], vcc
	v_add_u32_e32 v2, v4, v3
	v_mov_b32_e32 v3, 0x11988
	ds_write_b32 v3, v2
	s_or_b64 exec, exec, s[26:27]
	v_mov_b32_e32 v2, 0x11988
	s_waitcnt lgkmcnt(0)
	s_barrier
	ds_read_b32 v2, v2
	v_mov_b32_e32 v3, 0x11900
	s_and_b64 s[26:27], s[30:31], exec
	ds_read_b32 v5, v3
	s_cselect_b32 s26, 0xc3500, 0
	s_lshl_b32 s56, s26, 2
	s_add_u32 s28, s24, s56
	s_movk_i32 s24, 0x2001
	s_waitcnt lgkmcnt(1)
	v_cmp_gt_i32_e32 vcc, s24, v2
	v_readfirstlane_b32 s3, v2
	s_addc_u32 s29, s25, 0

.Lw1b10:
	s_mov_b64 s[34:35], -1
	s_cbranch_vccnz .LBB1_37
	s_mov_b64 s[24:25], 0
	v_mov_b32_e32 v3, 0x11880
	s_movk_i32 s36, 0x51
	s_movk_i32 s37, 0x52
	s_movk_i32 s38, 0x59
	s_movk_i32 s39, 0x5a
	s_movk_i32 s57, 0x5d
	s_movk_i32 s58, 0x5e
	s_movk_i32 s59, 0x5f
	s_movk_i32 s60, 0x60
	s_movk_i32 s61, 0x61
	v_mov_b32_e32 v4, 0x11990
	v_mov_b32_e32 v6, 1
	v_mov_b32_e32 v7, 0x11840
	v_mov_b32_e32 v8, 0x11820
	v_mov_b32_e32 v9, 0x11810
	v_mov_b32_e32 v10, 0x11808
	v_mov_b32_e32 v11, 0x11804
	v_mov_b32_e32 v12, 0x11800

.Lw1b11:
	v_mov_b32_e32 v13, v0
	s_branch .LBB1_16

.LBB1_18:
	s_or_b64 exec, exec, s[34:35]
	s_and_saveexec_b64 s[34:35], s[26:27]
.Lw1t13:
	s_cbranch_execz .Lw1c13
.Lw1b13:
	v_mov_b32_e32 v14, v15
	s_or_b64 exec, exec, s[34:35]
	v_cmp_lt_u32_e64 s[26:27], s38, v14
	v_cmp_gt_u32_e32 vcc, s39, v14
	s_and_saveexec_b64 s[34:35], vcc
	s_cbranch_execz .LBB1_22
	v_lshl_add_u32 v15, v14, 2, v8
	ds_read_b32 v16, v15
	s_andn2_b64 s[26:27], s[26:27], exec
	v_add_u32_e32 v15, 8, v14
	s_waitcnt lgkmcnt(0)
	v_cmp_gt_i32_e32 vcc, v16, v13
	s_and_b64 s[62:63], vcc, exec
	s_or_b64 s[26:27], s[26:27], s[62:63]
.LBB1_22:
	s_or_b64 exec, exec, s[34:35]
	s_and_saveexec_b64 s[34:35], s[26:27]
	v_mov_b32_e32 v15, v14
	s_or_b64 exec, exec, s[34:35]
	v_cmp_lt_u32_e64 s[26:27], s57, v15
	v_cmp_gt_u32_e32 vcc, s58, v15
	s_and_saveexec_b64 s[34:35], vcc
	s_cbranch_execz .LBB1_26
	v_lshl_add_u32 v14, v15, 2, v9
	ds_read_b32 v14, v14
	s_andn2_b64 s[26:27], s[26:27], exec
.Lw1t14:
	s_cbranch_execz .Lw1c14
.Lw1b14:
	v_add_u32_e32 v16, 4, v15
	s_waitcnt lgkmcnt(0)
	v_cmp_gt_i32_e32 vcc, v14, v13
	s_and_b64 s[62:63], vcc, exec
	s_or_b64 s[26:27], s[26:27], s[62:63]

.LBB1_37:
	s_load_dwordx4 s[24:27], s[0:1], 0x18
	s_movk_i32 s57, 0x2000
	s_and_b64 vcc, exec, s[34:35]
	s_cbranch_vccz .LBB1_231
	s_waitcnt lgkmcnt(0)
	s_load_dwordx4 s[68:71], s[0:1], 0x28
.Lw1t16:
	s_cbranch_execz .Lw1c16
.Lw1b16:
	s_and_b64 s[36:37], s[30:31], exec
	s_cselect_b32 s72, 0xc4, 0
	s_add_i32 s72, s72, s33
	s_addk_i32 s72, 0x190
	v_and_b32_e32 v48, 0x3c0, v0
	v_and_b32_e32 v49, 63, v0
	v_lshlrev_b32_e32 v58, 5, v48
	v_lshl_or_b32 v58, v49, 4, v58
	v_and_b32_e32 v59, 1, v0
	v_lshrrev_b32_e32 v49, 1, v49
	v_lshl_or_b32 v49, v59, 5, v49
	v_add_u32_e32 v49, v49, v48
	v_lshlrev_b32_e32 v49, 4, v49
	s_lshl_b32 s73, s72, 15
	s_waitcnt lgkmcnt(0)
	s_add_u32 s68, s68, s73
	s_addc_u32 s69, s69, 0
	s_mov_b32 s34, 0x11800
	s_movk_i32 s35, 0x62
	v_mov_b32_e32 v32, v0
	v_add_u32_e32 v33, 1024, v0
	v_add_u32_e32 v34, 2048, v0
	v_add_u32_e32 v35, 3072, v0

.Lw1b17:
	v_add_u32_e32 v36, 4096, v0
	v_add_u32_e32 v37, 5120, v0
	v_add_u32_e32 v38, 6144, v0
	v_add_u32_e32 v39, 7168, v0
	v_cmp_le_i32_e64 s[36:37], v5, v32
	v_cmp_le_i32_e64 s[38:39], v5, v33
	v_cmp_le_i32_e64 s[58:59], v5, v34
	v_cmp_le_i32_e64 s[60:61], v5, v35
	v_cndmask_b32_e64 v40, 0, 64, s[36:37]
	v_cndmask_b32_e64 v41, 0, 64, s[38:39]
	v_cndmask_b32_e64 v42, 0, 64, s[58:59]
	v_cndmask_b32_e64 v43, 0, 64, s[60:61]
	v_cmp_le_i32_e64 s[36:37], v5, v36
	v_cmp_le_i32_e64 s[38:39], v5, v37
	v_cmp_le_i32_e64 s[58:59], v5, v38
	v_cmp_le_i32_e64 s[60:61], v5, v39

.Lw1b18:
	v_cndmask_b32_e64 v44, 0, 64, s[36:37]
	v_cndmask_b32_e64 v45, 0, 64, s[38:39]
	v_cndmask_b32_e64 v46, 0, 64, s[58:59]
	v_cndmask_b32_e64 v47, 0, 64, s[60:61]
	v_add_u32_e32 v3, 32, v40
	v_lshl_add_u32 v11, v3, 2, s34
	ds_read_b32 v11, v11
	v_add_u32_e32 v4, 32, v41
	v_lshl_add_u32 v12, v4, 2, s34
	ds_read_b32 v12, v12
	v_add_u32_e32 v6, 32, v42
	v_lshl_add_u32 v13, v6, 2, s34
	ds_read_b32 v13, v13
	v_add_u32_e32 v7, 32, v43
	v_lshl_add_u32 v14, v7, 2, s34
	ds_read_b32 v14, v14
	v_add_u32_e32 v8, 32, v44
	v_lshl_add_u32 v15, v8, 2, s34

.Lw1b19:
	ds_read_b32 v15, v15
	v_add_u32_e32 v9, 32, v45
	v_lshl_add_u32 v16, v9, 2, s34
	ds_read_b32 v16, v16
	v_add_u32_e32 v10, 32, v46
	v_lshl_add_u32 v17, v10, 2, s34
	ds_read_b32 v17, v17
	v_add_u32_e32 v19, 32, v47
	v_lshl_add_u32 v18, v19, 2, s34
	ds_read_b32 v18, v18
	s_waitcnt lgkmcnt(7)
	v_cmp_le_i32_e64 s[36:37], v11, v32
	s_waitcnt lgkmcnt(6)
	v_cmp_le_i32_e64 s[38:39], v12, v33
	s_waitcnt lgkmcnt(5)
	v_cmp_le_i32_e64 s[58:59], v13, v34
	s_waitcnt lgkmcnt(4)
	v_cmp_le_i32_e64 s[60:61], v14, v35
	v_cndmask_b32_e64 v40, v40, v3, s[36:37]

.Lw1b20:
	v_cndmask_b32_e64 v41, v41, v4, s[38:39]
	v_cndmask_b32_e64 v42, v42, v6, s[58:59]
	v_cndmask_b32_e64 v43, v43, v7, s[60:61]
	s_waitcnt lgkmcnt(3)
	v_cmp_le_i32_e64 s[36:37], v15, v36
	s_waitcnt lgkmcnt(2)
	v_cmp_le_i32_e64 s[38:39], v16, v37
	s_waitcnt lgkmcnt(1)
	v_cmp_le_i32_e64 s[58:59], v17, v38
	s_waitcnt lgkmcnt(0)
	v_cmp_le_i32_e64 s[60:61], v18, v39
	v_cndmask_b32_e64 v44, v44, v8, s[36:37]
	v_cndmask_b32_e64 v45, v45, v9, s[38:39]
	v_cndmask_b32_e64 v46, v46, v10, s[58:59]
	v_cndmask_b32_e64 v47, v47, v19, s[60:61]
	v_add_u32_e32 v3, 16, v40
	v_min_u32_e32 v11, s35, v3
	v_lshl_add_u32 v11, v11, 2, s34

.Lw1b21:
	ds_read_b32 v11, v11
	v_add_u32_e32 v4, 16, v41
	v_min_u32_e32 v12, s35, v4
	v_lshl_add_u32 v12, v12, 2, s34
	ds_read_b32 v12, v12
	v_add_u32_e32 v6, 16, v42
	v_min_u32_e32 v13, s35, v6
	v_lshl_add_u32 v13, v13, 2, s34
	ds_read_b32 v13, v13
	v_add_u32_e32 v7, 16, v43
	v_min_u32_e32 v14, s35, v7
	v_lshl_add_u32 v14, v14, 2, s34
	ds_read_b32 v14, v14
	v_add_u32_e32 v8, 16, v44
	v_min_u32_e32 v15, s35, v8
	v_lshl_add_u32 v15, v15, 2, s34
	ds_read_b32 v15, v15
	v_add_u32_e32 v9, 16, v45
	v_min_u32_e32 v16, s35, v9
	v_lshl_add_u32 v16, v16, 2, s34
	ds_read_b32 v16, v16

.Lw1b22:
	v_add_u32_e32 v10, 16, v46
	v_min_u32_e32 v17, s35, v10
	v_lshl_add_u32 v17, v17, 2, s34
	ds_read_b32 v17, v17
	v_add_u32_e32 v19, 16, v47
	v_min_u32_e32 v18, s35, v19
	v_lshl_add_u32 v18, v18, 2, s34
	ds_read_b32 v18, v18
	s_waitcnt lgkmcnt(7)
	v_cmp_le_i32_e64 s[36:37], v11, v32
	s_waitcnt lgkmcnt(6)
	v_cmp_le_i32_e64 s[38:39], v12, v33
	s_waitcnt lgkmcnt(5)
	v_cmp_le_i32_e64 s[58:59], v13, v34
	s_waitcnt lgkmcnt(4)
	v_cmp_le_i32_e64 s[60:61], v14, v35
	v_cndmask_b32_e64 v40, v40, v3, s[36:37]
	v_cndmask_b32_e64 v41, v41, v4, s[38:39]
	v_cndmask_b32_e64 v42, v42, v6, s[58:59]

.Lw1b23:
	v_cndmask_b32_e64 v43, v43, v7, s[60:61]
	s_waitcnt lgkmcnt(3)
	v_cmp_le_i32_e64 s[36:37], v15, v36
	s_waitcnt lgkmcnt(2)
	v_cmp_le_i32_e64 s[38:39], v16, v37
	s_waitcnt lgkmcnt(1)
	v_cmp_le_i32_e64 s[58:59], v17, v38
	s_waitcnt lgkmcnt(0)
	v_cmp_le_i32_e64 s[60:61], v18, v39
	v_cndmask_b32_e64 v44, v44, v8, s[36:37]
	v_cndmask_b32_e64 v45, v45, v9, s[38:39]
	v_cndmask_b32_e64 v46, v46, v10, s[58:59]
	v_cndmask_b32_e64 v47, v47, v19, s[60:61]
	v_add_u32_e32 v3, 8, v40
	v_min_u32_e32 v11, s35, v3
	v_lshl_add_u32 v11, v11, 2, s34
	ds_read_b32 v11, v11
	v_add_u32_e32 v4, 8, v41
	v_min_u32_e32 v12, s35, v4
	v_lshl_add_u32 v12, v12, 2, s34

.Lw1b24:
	ds_read_b32 v12, v12
	v_add_u32_e32 v6, 8, v42
	v_min_u32_e32 v13, s35, v6
	v_lshl_add_u32 v13, v13, 2, s34
	ds_read_b32 v13, v13
	v_add_u32_e32 v7, 8, v43
	v_min_u32_e32 v14, s35, v7
	v_lshl_add_u32 v14, v14, 2, s34
	ds_read_b32 v14, v14
	v_add_u32_e32 v8, 8, v44
	v_min_u32_e32 v15, s35, v8
	v_lshl_add_u32 v15, v15, 2, s34
	ds_read_b32 v15, v15
	v_add_u32_e32 v9, 8, v45
	v_min_u32_e32 v16, s35, v9
	v_lshl_add_u32 v16, v16, 2, s34
	ds_read_b32 v16, v16
	v_add_u32_e32 v10, 8, v46
	v_min_u32_e32 v17, s35, v10
	v_lshl_add_u32 v17, v17, 2, s34

.Lw1b25:
	ds_read_b32 v17, v17
	v_add_u32_e32 v19, 8, v47
	v_min_u32_e32 v18, s35, v19
	v_lshl_add_u32 v18, v18, 2, s34
	ds_read_b32 v18, v18
	s_waitcnt lgkmcnt(7)
	v_cmp_le_i32_e64 s[36:37], v11, v32
	s_waitcnt lgkmcnt(6)
	v_cmp_le_i32_e64 s[38:39], v12, v33
	s_waitcnt lgkmcnt(5)
	v_cmp_le_i32_e64 s[58:59], v13, v34
	s_waitcnt lgkmcnt(4)
	v_cmp_le_i32_e64 s[60:61], v14, v35
	v_cndmask_b32_e64 v40, v40, v3, s[36:37]
	v_cndmask_b32_e64 v41, v41, v4, s[38:39]
	v_cndmask_b32_e64 v42, v42, v6, s[58:59]
	v_cndmask_b32_e64 v43, v43, v7, s[60:61]
	s_waitcnt lgkmcnt(3)
	v_cmp_le_i32_e64 s[36:37], v15, v36

.Lw1b26:
	s_waitcnt lgkmcnt(2)
	v_cmp_le_i32_e64 s[38:39], v16, v37
	s_waitcnt lgkmcnt(1)
	v_cmp_le_i32_e64 s[58:59], v17, v38
	s_waitcnt lgkmcnt(0)
	v_cmp_le_i32_e64 s[60:61], v18, v39
	v_cndmask_b32_e64 v44, v44, v8, s[36:37]
	v_cndmask_b32_e64 v45, v45, v9, s[38:39]
	v_cndmask_b32_e64 v46, v46, v10, s[58:59]
	v_cndmask_b32_e64 v47, v47, v19, s[60:61]
	v_add_u32_e32 v3, 4, v40
	v_min_u32_e32 v11, s35, v3
	v_lshl_add_u32 v11, v11, 2, s34
	ds_read_b32 v11, v11
	v_add_u32_e32 v4, 4, v41
	v_min_u32_e32 v12, s35, v4
	v_lshl_add_u32 v12, v12, 2, s34
	ds_read_b32 v12, v12
	v_add_u32_e32 v6, 4, v42
	v_min_u32_e32 v13, s35, v6

.Lw1b27:
	v_lshl_add_u32 v13, v13, 2, s34
	ds_read_b32 v13, v13
	v_add_u32_e32 v7, 4, v43
	v_min_u32_e32 v14, s35, v7
	v_lshl_add_u32 v14, v14, 2, s34
	ds_read_b32 v14, v14
	v_add_u32_e32 v8, 4, v44
	v_min_u32_e32 v15, s35, v8
	v_lshl_add_u32 v15, v15, 2, s34
	ds_read_b32 v15, v15
	v_add_u32_e32 v9, 4, v45
	v_min_u32_e32 v16, s35, v9
	v_lshl_add_u32 v16, v16, 2, s34
	ds_read_b32 v16, v16
	v_add_u32_e32 v10, 4, v46
	v_min_u32_e32 v17, s35, v10
	v_lshl_add_u32 v17, v17, 2, s34
	ds_read_b32 v17, v17
	v_add_u32_e32 v19, 4, v47
	v_min_u32_e32 v18, s35, v19
	v_lshl_add_u32 v18, v18, 2, s34

.Lw1b28:
	ds_read_b32 v18, v18
	s_waitcnt lgkmcnt(7)
	v_cmp_le_i32_e64 s[36:37], v11, v32
	s_waitcnt lgkmcnt(6)
	v_cmp_le_i32_e64 s[38:39], v12, v33
	s_waitcnt lgkmcnt(5)
	v_cmp_le_i32_e64 s[58:59], v13, v34
	s_waitcnt lgkmcnt(4)
	v_cmp_le_i32_e64 s[60:61], v14, v35
	v_cndmask_b32_e64 v40, v40, v3, s[36:37]
	v_cndmask_b32_e64 v41, v41, v4, s[38:39]
	v_cndmask_b32_e64 v42, v42, v6, s[58:59]
	v_cndmask_b32_e64 v43, v43, v7, s[60:61]
	s_waitcnt lgkmcnt(3)
	v_cmp_le_i32_e64 s[36:37], v15, v36
	s_waitcnt lgkmcnt(2)
	v_cmp_le_i32_e64 s[38:39], v16, v37
	s_waitcnt lgkmcnt(1)
	v_cmp_le_i32_e64 s[58:59], v17, v38

.Lw1b29:
	s_waitcnt lgkmcnt(0)
	v_cmp_le_i32_e64 s[60:61], v18, v39
	v_cndmask_b32_e64 v44, v44, v8, s[36:37]
	v_cndmask_b32_e64 v45, v45, v9, s[38:39]
	v_cndmask_b32_e64 v46, v46, v10, s[58:59]
	v_cndmask_b32_e64 v47, v47, v19, s[60:61]
	v_add_u32_e32 v3, 2, v40
	v_min_u32_e32 v11, s35, v3
	v_lshl_add_u32 v11, v11, 2, s34
	ds_read_b32 v11, v11
	v_add_u32_e32 v4, 2, v41
	v_min_u32_e32 v12, s35, v4
	v_lshl_add_u32 v12, v12, 2, s34
	ds_read_b32 v12, v12
	v_add_u32_e32 v6, 2, v42
	v_min_u32_e32 v13, s35, v6
	v_lshl_add_u32 v13, v13, 2, s34
	ds_read_b32 v13, v13
	v_add_u32_e32 v7, 2, v43

.Lw1b30:
	v_min_u32_e32 v14, s35, v7
	v_lshl_add_u32 v14, v14, 2, s34
	ds_read_b32 v14, v14
	v_add_u32_e32 v8, 2, v44
	v_min_u32_e32 v15, s35, v8
	v_lshl_add_u32 v15, v15, 2, s34
	ds_read_b32 v15, v15
	v_add_u32_e32 v9, 2, v45
	v_min_u32_e32 v16, s35, v9
	v_lshl_add_u32 v16, v16, 2, s34
	ds_read_b32 v16, v16
	v_add_u32_e32 v10, 2, v46
	v_min_u32_e32 v17, s35, v10
	v_lshl_add_u32 v17, v17, 2, s34
	ds_read_b32 v17, v17
	v_add_u32_e32 v19, 2, v47
	v_min_u32_e32 v18, s35, v19
	v_lshl_add_u32 v18, v18, 2, s34
	ds_read_b32 v18, v18
	s_waitcnt lgkmcnt(7)
	v_cmp_le_i32_e64 s[36:37], v11, v32

.Lw1b31:
	s_waitcnt lgkmcnt(6)
	v_cmp_le_i32_e64 s[38:39], v12, v33
	s_waitcnt lgkmcnt(5)
	v_cmp_le_i32_e64 s[58:59], v13, v34
	s_waitcnt lgkmcnt(4)
	v_cmp_le_i32_e64 s[60:61], v14, v35
	v_cndmask_b32_e64 v40, v40, v3, s[36:37]
	v_cndmask_b32_e64 v41, v41, v4, s[38:39]
	v_cndmask_b32_e64 v42, v42, v6, s[58:59]
	v_cndmask_b32_e64 v43, v43, v7, s[60:61]
	s_waitcnt lgkmcnt(3)
	v_cmp_le_i32_e64 s[36:37], v15, v36
	s_waitcnt lgkmcnt(2)
	v_cmp_le_i32_e64 s[38:39], v16, v37
	s_waitcnt lgkmcnt(1)
	v_cmp_le_i32_e64 s[58:59], v17, v38
	s_waitcnt lgkmcnt(0)
	v_cmp_le_i32_e64 s[60:61], v18, v39
	v_cndmask_b32_e64 v44, v44, v8, s[36:37]

.Lw1b32:
	v_cndmask_b32_e64 v45, v45, v9, s[38:39]
	v_cndmask_b32_e64 v46, v46, v10, s[58:59]
	v_cndmask_b32_e64 v47, v47, v19, s[60:61]
	v_add_u32_e32 v3, 1, v40
	v_min_u32_e32 v11, s35, v3
	v_lshl_add_u32 v11, v11, 2, s34
	ds_read_b32 v11, v11
	v_add_u32_e32 v4, 1, v41
	v_min_u32_e32 v12, s35, v4
	v_lshl_add_u32 v12, v12, 2, s34
	ds_read_b32 v12, v12
	v_add_u32_e32 v6, 1, v42
	v_min_u32_e32 v13, s35, v6
	v_lshl_add_u32 v13, v13, 2, s34
	ds_read_b32 v13, v13
	v_add_u32_e32 v7, 1, v43
	v_min_u32_e32 v14, s35, v7
	v_lshl_add_u32 v14, v14, 2, s34
	ds_read_b32 v14, v14

.Lw1b33:
	v_add_u32_e32 v8, 1, v44
	v_min_u32_e32 v15, s35, v8
	v_lshl_add_u32 v15, v15, 2, s34
	ds_read_b32 v15, v15
	v_add_u32_e32 v9, 1, v45
	v_min_u32_e32 v16, s35, v9
	v_lshl_add_u32 v16, v16, 2, s34
	ds_read_b32 v16, v16
	v_add_u32_e32 v10, 1, v46
	v_min_u32_e32 v17, s35, v10
	v_lshl_add_u32 v17, v17, 2, s34
	ds_read_b32 v17, v17
	v_add_u32_e32 v19, 1, v47
	v_min_u32_e32 v18, s35, v19
	v_lshl_add_u32 v18, v18, 2, s34
	ds_read_b32 v18, v18
	s_waitcnt lgkmcnt(7)
	v_cmp_le_i32_e64 s[36:37], v11, v32
	s_waitcnt lgkmcnt(6)
	v_cmp_le_i32_e64 s[38:39], v12, v33
	s_waitcnt lgkmcnt(5)

.Lw1b34:
	v_cmp_le_i32_e64 s[58:59], v13, v34
	s_waitcnt lgkmcnt(4)
	v_cmp_le_i32_e64 s[60:61], v14, v35
	v_cndmask_b32_e64 v40, v40, v3, s[36:37]
	v_cndmask_b32_e64 v41, v41, v4, s[38:39]
	v_cndmask_b32_e64 v42, v42, v6, s[58:59]
	v_cndmask_b32_e64 v43, v43, v7, s[60:61]
	s_waitcnt lgkmcnt(3)
	v_cmp_le_i32_e64 s[36:37], v15, v36
	s_waitcnt lgkmcnt(2)
	v_cmp_le_i32_e64 s[38:39], v16, v37
	s_waitcnt lgkmcnt(1)
	v_cmp_le_i32_e64 s[58:59], v17, v38
	s_waitcnt lgkmcnt(0)
	v_cmp_le_i32_e64 s[60:61], v18, v39
	v_cndmask_b32_e64 v44, v44, v8, s[36:37]
	v_cndmask_b32_e64 v45, v45, v9, s[38:39]
	v_cndmask_b32_e64 v46, v46, v10, s[58:59]

.Lw1b35:
	v_cndmask_b32_e64 v47, v47, v19, s[60:61]
	v_lshl_add_u32 v11, v40, 2, s34
	ds_read_b32 v3, v11
	ds_read_b32 v11, v11 offset:400
	v_lshl_add_u32 v12, v41, 2, s34
	ds_read_b32 v4, v12
	ds_read_b32 v12, v12 offset:400
	v_lshl_add_u32 v13, v42, 2, s34
	ds_read_b32 v6, v13
	ds_read_b32 v13, v13 offset:400
	v_lshl_add_u32 v14, v43, 2, s34
	ds_read_b32 v7, v14
	ds_read_b32 v14, v14 offset:400
	v_lshl_add_u32 v15, v44, 2, s34
	ds_read_b32 v8, v15
	ds_read_b32 v15, v15 offset:400

.Lw1b36:
	v_lshl_add_u32 v16, v45, 2, s34
	ds_read_b32 v9, v16
	ds_read_b32 v16, v16 offset:400
	v_lshl_add_u32 v17, v46, 2, s34
	ds_read_b32 v10, v17
	ds_read_b32 v17, v17 offset:400
	v_lshl_add_u32 v18, v47, 2, s34
	ds_read_b32 v19, v18
	ds_read_b32 v18, v18 offset:400
	s_waitcnt lgkmcnt(14)
	v_sub_u32_e32 v3, v32, v3
	v_lshl_add_u32 v40, v40, 13, v3
	v_add_lshl_u32 v40, v40, v11, 2
	s_waitcnt lgkmcnt(12)
	v_sub_u32_e32 v4, v33, v4
	v_lshl_add_u32 v41, v41, 13, v4
	v_add_lshl_u32 v41, v41, v12, 2

.Lw1b37:
	s_waitcnt lgkmcnt(10)
	v_sub_u32_e32 v6, v34, v6
	v_lshl_add_u32 v42, v42, 13, v6
	v_add_lshl_u32 v42, v42, v13, 2
	s_waitcnt lgkmcnt(8)
	v_sub_u32_e32 v7, v35, v7
	v_lshl_add_u32 v43, v43, 13, v7
	v_add_lshl_u32 v43, v43, v14, 2
	s_waitcnt lgkmcnt(6)
	v_sub_u32_e32 v8, v36, v8
	v_lshl_add_u32 v44, v44, 13, v8
	v_add_lshl_u32 v44, v44, v15, 2
	s_waitcnt lgkmcnt(4)
	v_sub_u32_e32 v9, v37, v9
	v_lshl_add_u32 v45, v45, 13, v9
	v_add_lshl_u32 v45, v45, v16, 2
	s_waitcnt lgkmcnt(2)
	v_sub_u32_e32 v10, v38, v10
	v_lshl_add_u32 v46, v46, 13, v10
	v_add_lshl_u32 v46, v46, v17, 2
	s_waitcnt lgkmcnt(0)

.Lw1b38:
	v_sub_u32_e32 v19, v39, v19
	v_lshl_add_u32 v47, v47, 13, v19
	v_add_lshl_u32 v47, v47, v18, 2
	v_cmp_gt_i32_e64 s[36:37], s3, v32
	v_mov_b32_e32 v3, -1
	s_mov_b64 exec, s[36:37]
	global_load_dword v3, v40, s[28:29]
	s_mov_b64 exec, -1
	v_cmp_gt_i32_e64 s[38:39], s3, v33
	v_mov_b32_e32 v4, -1
	s_mov_b64 exec, s[38:39]
	global_load_dword v4, v41, s[28:29]
	s_mov_b64 exec, -1
	v_cmp_gt_i32_e64 s[58:59], s3, v34
	v_mov_b32_e32 v6, -1
	s_mov_b64 exec, s[58:59]
	global_load_dword v6, v42, s[28:29]
	s_mov_b64 exec, -1
	v_cmp_gt_i32_e64 s[60:61], s3, v35
	v_mov_b32_e32 v7, -1
	s_mov_b64 exec, s[60:61]
	global_load_dword v7, v43, s[28:29]

.Lw1b39:
	s_mov_b64 exec, -1
	v_cmp_gt_i32_e64 s[36:37], s3, v36
	v_mov_b32_e32 v8, -1
	s_mov_b64 exec, s[36:37]
	global_load_dword v8, v44, s[28:29]
	s_mov_b64 exec, -1
	v_cmp_gt_i32_e64 s[38:39], s3, v37
	v_mov_b32_e32 v9, -1
	s_mov_b64 exec, s[38:39]
	global_load_dword v9, v45, s[28:29]
	s_mov_b64 exec, -1
	v_cmp_gt_i32_e64 s[58:59], s3, v38
	v_mov_b32_e32 v10, -1
	s_mov_b64 exec, s[58:59]
	global_load_dword v10, v46, s[28:29]
	s_mov_b64 exec, -1
	v_cmp_gt_i32_e64 s[60:61], s3, v39
	v_mov_b32_e32 v13, -1
	s_mov_b64 exec, s[60:61]
	global_load_dword v13, v47, s[28:29]
	s_mov_b64 exec, -1
	global_load_dwordx4 v[50:53], v58, s[68:69] nt

.Lw1b40:
	global_load_dwordx4 v[54:57], v58, s[68:69] offset:1024 nt
	v_mov_b32_e32 v19, 1
	s_waitcnt vmcnt(9)
	v_cmp_ne_u32_e64 s[36:37], -1, v3
	v_lshrrev_b32_e32 v32, 15, v3
	v_and_b32_e32 v32, 0x1fffc, v32
	v_add_u32_e32 v32, 0x10000, v32
	v_mov_b32_e32 v15, 0
	s_mov_b64 exec, s[36:37]
	ds_add_rtn_u32 v15, v32, v19
	s_mov_b64 exec, -1
	s_waitcnt vmcnt(8)
	v_cmp_ne_u32_e64 s[38:39], -1, v4
	v_lshrrev_b32_e32 v33, 15, v4
	v_and_b32_e32 v33, 0x1fffc, v33
	v_add_u32_e32 v33, 0x10000, v33
	v_mov_b32_e32 v5, 0
	s_mov_b64 exec, s[38:39]
	ds_add_rtn_u32 v5, v33, v19
	s_mov_b64 exec, -1
	s_waitcnt vmcnt(7)

.Lw1b41:
	v_cmp_ne_u32_e64 s[58:59], -1, v6
	v_lshrrev_b32_e32 v34, 15, v6
	v_and_b32_e32 v34, 0x1fffc, v34
	v_add_u32_e32 v34, 0x10000, v34
	v_mov_b32_e32 v16, 0
	s_mov_b64 exec, s[58:59]
	ds_add_rtn_u32 v16, v34, v19
	s_mov_b64 exec, -1
	s_waitcnt vmcnt(6)
	v_cmp_ne_u32_e64 s[60:61], -1, v7
	v_lshrrev_b32_e32 v35, 15, v7
	v_and_b32_e32 v35, 0x1fffc, v35
	v_add_u32_e32 v35, 0x10000, v35
	v_mov_b32_e32 v11, 0
	s_mov_b64 exec, s[60:61]
	ds_add_rtn_u32 v11, v35, v19
	s_mov_b64 exec, -1
	s_waitcnt vmcnt(5)
	v_cmp_ne_u32_e64 s[36:37], -1, v8
	v_lshrrev_b32_e32 v36, 15, v8
	v_and_b32_e32 v36, 0x1fffc, v36

.Lw1b42:
	v_add_u32_e32 v36, 0x10000, v36
	v_mov_b32_e32 v17, 0
	s_mov_b64 exec, s[36:37]
	ds_add_rtn_u32 v17, v36, v19
	s_mov_b64 exec, -1
	s_waitcnt vmcnt(4)
	v_cmp_ne_u32_e64 s[38:39], -1, v9
	v_lshrrev_b32_e32 v37, 15, v9
	v_and_b32_e32 v37, 0x1fffc, v37
	v_add_u32_e32 v37, 0x10000, v37
	v_mov_b32_e32 v12, 0
	s_mov_b64 exec, s[38:39]
	ds_add_rtn_u32 v12, v37, v19
	s_mov_b64 exec, -1
	s_waitcnt vmcnt(3)
	v_cmp_ne_u32_e64 s[58:59], -1, v10
	v_lshrrev_b32_e32 v38, 15, v10
	v_and_b32_e32 v38, 0x1fffc, v38
	v_add_u32_e32 v38, 0x10000, v38
	v_mov_b32_e32 v18, 0
	s_mov_b64 exec, s[58:59]
	ds_add_rtn_u32 v18, v38, v19

.Lw1b43:
	s_mov_b64 exec, -1
	s_waitcnt vmcnt(2)
	v_cmp_ne_u32_e64 s[60:61], -1, v13
	v_lshrrev_b32_e32 v39, 15, v13
	v_and_b32_e32 v39, 0x1fffc, v39
	v_add_u32_e32 v39, 0x10000, v39
	v_mov_b32_e32 v14, 0
	s_mov_b64 exec, s[60:61]
	ds_add_rtn_u32 v14, v39, v19
	s_mov_b64 exec, -1
	s_waitcnt vmcnt(0)
	s_lshl_b32 s73, s72, 14
	s_add_u32 s70, s70, s73
	s_addc_u32 s71, s71, 0
	v_cmp_eq_u32_e64 s[36:37], 0, v59
	v_cvt_pk_f16_f32 v50, v50, v51
	v_cvt_pk_f16_f32 v51, v52, v53
	v_cvt_pk_f16_f32 v52, v54, v55
	v_cvt_pk_f16_f32 v53, v56, v57
	v_cndmask_b32_e64 v54, v50, v52, s[36:37]

.Lw1b44:
	v_cndmask_b32_e64 v55, v51, v53, s[36:37]
	s_nop 1
	v_mov_b32_dpp v54, v54 quad_perm:[1,0,3,2] row_mask:0xf bank_mask:0xf bound_ctrl:1
	v_mov_b32_dpp v55, v55 quad_perm:[1,0,3,2] row_mask:0xf bank_mask:0xf bound_ctrl:1
	v_cndmask_b32_e64 v50, v54, v50, s[36:37]
	v_cndmask_b32_e64 v51, v55, v51, s[36:37]
	v_cndmask_b32_e64 v52, v52, v54, s[36:37]
	v_cndmask_b32_e64 v53, v53, v55, s[36:37]
	global_store_dwordx4 v49, v[50:53], s[70:71] sc1
	s_branch .LBB1_232

.LBB1_232:
	v_cmp_lt_i32_e32 vcc, s57, v2
	v_mov_b32_e32 v2, 0
	s_waitcnt lgkmcnt(0)
	s_barrier
	s_and_saveexec_b64 s[34:35], s[22:23]
.Lw1t45:
	s_cbranch_execz .Lw1c45
.Lw1b45:
	v_mov_b32_e32 v2, 0x10000
	v_lshl_or_b32 v2, v0, 2, v2
	ds_read_b32 v2, v2
	s_or_b64 exec, exec, s[34:35]
	s_waitcnt lgkmcnt(0)
	v_add_u32_dpp v19, v2, v2 row_shr:1 row_mask:0xf bank_mask:0xf bound_ctrl:1
	s_nop 1
	v_add_u32_dpp v19, v19, v19 row_shr:2 row_mask:0xf bank_mask:0xf bound_ctrl:1
	s_nop 1
	v_add_u32_dpp v19, v19, v19 row_shr:4 row_mask:0xf bank_mask:0xf bound_ctrl:1
	s_nop 1
	v_add_u32_dpp v19, v19, v19 row_shr:8 row_mask:0xf bank_mask:0xf bound_ctrl:1
	s_nop 1
	v_add_u32_dpp v19, v19, v19 row_bcast:15 row_mask:0xa bank_mask:0xf
	s_nop 1
	v_add_u32_dpp v19, v19, v19 row_bcast:31 row_mask:0xc bank_mask:0xf
	s_and_saveexec_b64 s[34:35], s[4:5]
	v_mov_b32_e32 v20, 0x11b60
	v_lshl_add_u32 v1, v1, 2, v20
	ds_write_b32 v1, v19

.Lw1b46:
	s_or_b64 exec, exec, s[34:35]
	s_add_i32 s41, s41, s40
	s_add_i32 s42, s42, s41
	s_add_i32 s43, s43, s42
	s_add_i32 s44, s44, s43
	s_add_i32 s45, s45, s44
	s_add_i32 s46, s46, s45
	s_add_i32 s47, s47, s46
	s_add_i32 s48, s48, s47
	s_add_i32 s49, s49, s48
	s_add_i32 s50, s50, s49
	s_add_i32 s51, s51, s50
	s_add_i32 s52, s52, s51
	s_add_i32 s53, s53, s52
	s_add_i32 s54, s54, s53
	s_add_i32 s34, s55, s54
	s_waitcnt lgkmcnt(0)
	s_barrier
	s_and_saveexec_b64 s[36:37], s[22:23]
	s_cbranch_execz .LBB1_239
	v_mov_b32_e32 v1, 0x11b98
	v_mov_b32_e32 v20, 0x11b70
	ds_read_b32 v1, v1
	ds_read_b96 v[24:26], v20
	v_mov_b32_e32 v20, 0x11b60

.Lw1b47:
	ds_read_b128 v[20:23], v20
	v_sub_u32_e32 v2, v19, v2
	s_waitcnt lgkmcnt(2)
	v_cndmask_b32_e64 v1, 0, v1, s[20:21]
	s_waitcnt lgkmcnt(1)
	v_cndmask_b32_e64 v24, 0, v24, s[14:15]
	v_cndmask_b32_e64 v26, 0, v26, s[18:19]
	s_waitcnt lgkmcnt(0)
	v_cndmask_b32_e64 v22, 0, v22, s[10:11]
	v_cndmask_b32_e64 v21, 0, v21, s[8:9]
	v_cndmask_b32_e64 v20, v20, 0, s[6:7]
	v_cndmask_b32_e64 v23, 0, v23, s[12:13]
	v_add3_u32 v20, v21, v20, v22
	v_cndmask_b32_e64 v25, 0, v25, s[16:17]
	v_add3_u32 v20, v23, v20, v24
	v_add3_u32 v20, v25, v20, v26
	v_add3_u32 v1, v1, v20, v2
	v_mov_b32_e32 v2, 0x11000

.Lw1b48:
	v_lshl_or_b32 v2, v0, 2, v2
	ds_write_b32 v2, v1
	v_lshl_or_b32 v2, s33, 9, v0
	s_mov_b32 s4, 0x186a0
	v_cmp_gt_u32_e64 s[4:5], s4, v2
	s_and_b64 exec, exec, s[4:5]
	s_cbranch_execz .LBB1_239
	s_and_b64 s[4:5], s[30:31], exec
	s_cselect_b32 s4, 0x186a1, 0
	v_add_u32_e32 v20, s4, v2
	v_mov_b32_e32 v21, 0
	v_lshl_add_u64 v[20:21], v[20:21], 2, s[24:25]
	v_add_u32_e32 v1, s34, v1
	global_store_dword v[20:21], v1, off

.LBB1_241:
	s_or_b64 exec, exec, s[4:5]
	s_add_u32 s6, s26, s56
	s_addc_u32 s7, s27, 0
	s_ashr_i32 s35, s34, 31
	s_lshl_b64 s[4:5], s[34:35], 2
	s_add_u32 s8, s6, s4
	s_addc_u32 s9, s7, s5
	s_mov_b64 s[4:5], -1
	s_and_b64 vcc, exec, vcc
	s_waitcnt lgkmcnt(0)
	s_barrier
	s_cbranch_vccz .LBB1_265
	v_mov_b32_e32 v1, 0x11900
	ds_read_b32 v1, v1
	s_mov_b64 s[4:5], 0
	v_mov_b32_e32 v2, 0x11880
	s_movk_i32 s12, 0x51
.Lw1t50:
	s_cbranch_execz .Lw1c50
.Lw1b50:
	s_movk_i32 s13, 0x52
	s_movk_i32 s14, 0x59
	s_movk_i32 s15, 0x5a
	s_movk_i32 s16, 0x5d
	s_movk_i32 s17, 0x5e
	s_movk_i32 s18, 0x5f
	s_movk_i32 s19, 0x60
	s_movk_i32 s20, 0x61
	v_mov_b32_e32 v19, 0x11990
	v_mov_b32_e32 v20, 1
	v_mov_b32_e32 v21, 0x11840
	v_mov_b32_e32 v22, 0x11820
	v_mov_b32_e32 v23, 0x11810
	v_mov_b32_e32 v24, 0x11808
	v_mov_b32_e32 v25, 0x11804
	v_mov_b32_e32 v26, 0x11800
	v_mov_b32_e32 v27, v0
	s_branch .LBB1_244
.LBB1_243:
	s_or_b64 exec, exec, s[10:11]
	v_lshl_add_u32 v28, v30, 2, v19
	ds_read_b32 v28, v28
	s_waitcnt lgkmcnt(0)
.Lw1t51:
	s_cbranch_execz .Lw1c51
.Lw1b51:
	v_lshl_add_u32 v28, v30, 13, v28
	v_sub_u32_e32 v28, v28, v29
	v_add_u32_e32 v28, v27, v28
	v_ashrrev_i32_e32 v29, 31, v28
	v_lshl_add_u64 v[28:29], v[28:29], 2, s[28:29]
	global_load_dword v28, v[28:29], off
	v_add_u32_e32 v27, 0x400, v27
	v_cmp_le_i32_e32 vcc, s3, v27
	s_or_b64 s[4:5], vcc, s[4:5]
	s_waitcnt vmcnt(0)
	v_lshrrev_b32_e32 v29, 15, v28
	v_and_b32_e32 v29, 0x1fffc, v29
	v_add_u32_e32 v30, 0x11000, v29
	v_add_u32_e32 v29, 0x10800, v29
	ds_read_b32 v30, v30
	ds_add_rtn_u32 v29, v29, v20
	v_and_b32_e32 v31, 0x1fffff, v28
	s_waitcnt lgkmcnt(0)
	v_add_u32_e32 v28, v29, v30
	v_ashrrev_i32_e32 v29, 31, v28
	v_lshl_add_u64 v[28:29], v[28:29], 2, s[8:9]

.Lw1b52:
	global_store_dword v[28:29], v31, off
	s_andn2_b64 exec, exec, s[4:5]
	s_cbranch_execz .LBB1_264
.LBB1_244:
	s_waitcnt lgkmcnt(0)
	v_cmp_gt_i32_e32 vcc, v1, v27
	s_nop 1
	v_cndmask_b32_e64 v28, 64, 0, vcc
	v_lshl_or_b32 v29, v28, 2, v2
	ds_read_b32 v29, v29
	v_or_b32_e32 v30, 32, v28
	s_waitcnt lgkmcnt(0)
	v_cmp_gt_i32_e32 vcc, v29, v27
	s_nop 1
	v_cndmask_b32_e32 v29, v30, v28, vcc
	v_cmp_lt_u32_e64 s[6:7], s12, v29
	v_cmp_gt_u32_e32 vcc, s13, v29
	s_and_saveexec_b64 s[10:11], vcc
	s_cbranch_execz .LBB1_246
	v_lshl_add_u32 v28, v29, 2, v21
	ds_read_b32 v30, v28
	s_andn2_b64 s[6:7], s[6:7], exec
	v_or_b32_e32 v28, 16, v29
	s_waitcnt lgkmcnt(0)

.Lw1b53:
	v_cmp_gt_i32_e32 vcc, v30, v27
	s_and_b64 s[22:23], vcc, exec
	s_or_b64 s[6:7], s[6:7], s[22:23]

.Lw1b55:
	v_mov_b32_e32 v28, v30
	s_or_b64 exec, exec, s[10:11]
	v_cmp_lt_u32_e64 s[6:7], s19, v28
	v_cmp_gt_u32_e32 vcc, s20, v28
	s_and_saveexec_b64 s[10:11], vcc
	s_cbranch_execz .LBB1_262
	v_lshl_add_u32 v29, v28, 2, v25
	ds_read_b32 v29, v29
	s_andn2_b64 s[6:7], s[6:7], exec
	v_add_u32_e32 v30, 1, v28
	s_waitcnt lgkmcnt(0)
	v_cmp_gt_i32_e32 vcc, v29, v27
	s_and_b64 s[22:23], vcc, exec
	s_or_b64 s[6:7], s[6:7], s[22:23]

.LBB1_265:
	s_and_b64 vcc, exec, s[4:5]
	s_cbranch_vccz .LBB1_390
	v_cmp_ne_u32_e32 vcc, -1, v3
.Lw1t56:
	s_cbranch_execz .Lw1c56
.Lw1b56:
	s_and_saveexec_b64 s[4:5], vcc
	s_cbranch_execz .LBB1_274
	v_lshrrev_b32_e32 v1, 15, v3
	v_and_b32_e32 v1, 0x1fffc, v1
	v_add_u32_e32 v1, 0x11000, v1
	ds_read_b32 v1, v1
	v_lshlrev_b32_e32 v2, 2, v15
	s_waitcnt lgkmcnt(0)
	v_lshl_add_u32 v1, v1, 2, v2
	ds_write_b32 v1, v3
	s_or_b64 exec, exec, s[4:5]
	v_cmp_ne_u32_e32 vcc, -1, v4
	s_and_saveexec_b64 s[4:5], vcc
	s_cbranch_execnz .LBB1_275

.LBB1_269:
	v_lshrrev_b32_e32 v1, 15, v6
	v_and_b32_e32 v1, 0x1fffc, v1
	v_add_u32_e32 v1, 0x11000, v1
	ds_read_b32 v1, v1
	v_lshlrev_b32_e32 v2, 2, v16
.Lw1t57:
	s_cbranch_execz .Lw1c57
.Lw1b57:
	s_waitcnt lgkmcnt(0)
	v_lshl_add_u32 v1, v1, 2, v2
	ds_write_b32 v1, v6
	s_or_b64 exec, exec, s[4:5]
	v_cmp_ne_u32_e32 vcc, -1, v7
	s_and_saveexec_b64 s[4:5], vcc
	s_cbranch_execnz .LBB1_277

.LBB1_275:
	v_lshrrev_b32_e32 v1, 15, v4
	v_and_b32_e32 v1, 0x1fffc, v1
	v_add_u32_e32 v1, 0x11000, v1
	ds_read_b32 v1, v1
.Lw1t59:
	s_cbranch_execz .Lw1c59
.Lw1b59:
	v_lshlrev_b32_e32 v2, 2, v5
	s_waitcnt lgkmcnt(0)
	v_lshl_add_u32 v1, v1, 2, v2
	ds_write_b32 v1, v4
	s_or_b64 exec, exec, s[4:5]
	v_cmp_ne_u32_e32 vcc, -1, v6
	s_and_saveexec_b64 s[4:5], vcc
	s_cbranch_execnz .LBB1_269

.LBB1_277:
	v_lshrrev_b32_e32 v1, 15, v7
	v_and_b32_e32 v1, 0x1fffc, v1
	v_add_u32_e32 v1, 0x11000, v1
	ds_read_b32 v1, v1
	v_lshlrev_b32_e32 v2, 2, v11
	s_waitcnt lgkmcnt(0)
	v_lshl_add_u32 v1, v1, 2, v2
	ds_write_b32 v1, v7
	s_or_b64 exec, exec, s[4:5]
	v_cmp_ne_u32_e32 vcc, -1, v8
	s_and_saveexec_b64 s[4:5], vcc
.Lw1t60:
	s_cbranch_execz .Lw1c60

.LBB1_281:
	v_lshrrev_b32_e32 v1, 15, v13
	v_and_b32_e32 v1, 0x1fffc, v1
	v_add_u32_e32 v1, 0x11000, v1
.Lw1t61:
	s_cbranch_execz .Lw1c61
.Lw1b61:
	ds_read_b32 v1, v1
	v_lshlrev_b32_e32 v2, 2, v14
	s_waitcnt lgkmcnt(0)
	v_lshl_add_u32 v1, v1, 2, v2
	ds_write_b32 v1, v13
.LBB1_282:
	s_or_b64 exec, exec, s[4:5]
	v_mov_b32_e32 v1, 0x11ba0
	v_mov_b32_e32 v2, -1
	ds_write_b32 v1, v2
	s_cmp_lt_i32 s3, 1
	s_waitcnt lgkmcnt(0)
	s_barrier
	s_cbranch_scc1 .LBB1_332
	v_lshlrev_b32_e32 v1, 2, v0
	s_lshl_b32 s18, s3, 2
	s_mov_b32 s19, 0x1fffc
	s_mov_b32 s20, 0x10000
	v_mov_b32_e32 v7, 0x11ba0
	v_mov_b32_e32 v2, v0
	v_cmp_gt_i32_e64 s[10:11], s3, v2
	ds_read_b32 v17, v1

.Lw1b62:
	v_mov_b32_e32 v16, v1
	v_add_u32_e32 v2, 1024, v0
	v_cmp_gt_i32_e64 s[12:13], s3, v2
	ds_read_b32 v19, v1 offset:4096
	v_add_u32_e32 v18, 4096, v1
	v_add_u32_e32 v2, 2048, v0
	v_cmp_gt_i32_e64 s[14:15], s3, v2
	ds_read_b32 v21, v1 offset:8192
	v_add_u32_e32 v20, 8192, v1
	v_add_u32_e32 v2, 3072, v0
	v_cmp_gt_i32_e64 s[16:17], s3, v2
	ds_read_b32 v23, v1 offset:12288
	v_add_u32_e32 v22, 12288, v1
	s_waitcnt lgkmcnt(0)
	v_lshrrev_b32_e32 v2, 15, v17
	v_and_b32_e32 v2, s19, v2
	v_lshrrev_b32_e32 v3, 15, v19
	v_and_b32_e32 v3, s19, v3
	v_lshrrev_b32_e32 v4, 15, v21

.Lw1b63:
	v_and_b32_e32 v4, s19, v4
	v_lshrrev_b32_e32 v5, 15, v23
	v_and_b32_e32 v5, s19, v5
	v_cndmask_b32_e64 v2, 0, v2, s[10:11]
	v_add_u32_e32 v2, s20, v2
	v_cndmask_b32_e64 v3, 0, v3, s[12:13]
	v_add_u32_e32 v3, s20, v3
	v_cndmask_b32_e64 v4, 0, v4, s[14:15]
	v_add_u32_e32 v4, s20, v4
	v_cndmask_b32_e64 v5, 0, v5, s[16:17]
	v_add_u32_e32 v5, s20, v5
	ds_read_b32 v24, v2
	ds_read_b32 v28, v2 offset:4096
	ds_read_b32 v25, v3
	ds_read_b32 v29, v3 offset:4096
	ds_read_b32 v26, v4
	ds_read_b32 v30, v4 offset:4096
	ds_read_b32 v27, v5
	ds_read_b32 v31, v5 offset:4096

.Lw1b64:
	s_waitcnt lgkmcnt(0)
	v_cndmask_b32_e64 v2, 0, v24, s[10:11]
	v_lshlrev_b32_e32 v28, 2, v28
	v_mov_b32_e32 v8, v28
	v_mov_b32_e32 v24, 0
	v_cndmask_b32_e64 v3, 0, v25, s[12:13]
	v_lshlrev_b32_e32 v29, 2, v29
	v_mov_b32_e32 v10, v29
	v_mov_b32_e32 v25, 0
	v_cndmask_b32_e64 v4, 0, v26, s[14:15]
	v_lshlrev_b32_e32 v30, 2, v30
	v_mov_b32_e32 v12, v30
	v_mov_b32_e32 v26, 0
	v_cndmask_b32_e64 v5, 0, v27, s[16:17]
	v_lshlrev_b32_e32 v31, 2, v31
	v_mov_b32_e32 v14, v31
	v_mov_b32_e32 v27, 0
	v_max_u32_e32 v6, v2, v3
	v_max3_u32 v6, v6, v4, v5
	s_mov_b32 s21, 0
.Lrs0_loop:
	v_cmp_lt_u32_e32 vcc, s21, v6
	s_cbranch_vccz .Lrs0_done
	v_cmp_gt_u32_e64 s[22:23], s18, v8
	v_cmp_gt_u32_e64 s[24:25], s18, v10
.Lw1t65:
	s_cbranch_execz .Lw1c65
.Lw1b65:
	v_cmp_gt_u32_e64 s[26:27], s18, v12
	v_cmp_gt_u32_e64 s[28:29], s18, v14
	v_cndmask_b32_e64 v2, v7, v8, s[22:23]
	v_cndmask_b32_e64 v3, v7, v10, s[24:25]
	v_cndmask_b32_e64 v4, v7, v12, s[26:27]
	v_cndmask_b32_e64 v5, v7, v14, s[28:29]
	ds_read_b32 v9, v2
	ds_read_b32 v11, v3
	ds_read_b32 v13, v4
	ds_read_b32 v15, v5
	s_waitcnt lgkmcnt(3)
	v_cmp_lt_u64_e64 s[22:23], v[8:9], v[16:17]
	s_waitcnt lgkmcnt(2)
	v_cmp_lt_u64_e64 s[24:25], v[10:11], v[18:19]
	s_waitcnt lgkmcnt(1)
	v_cmp_lt_u64_e64 s[26:27], v[12:13], v[20:21]
	s_waitcnt lgkmcnt(0)
	v_cmp_lt_u64_e64 s[28:29], v[14:15], v[22:23]

.Lw1b66:
	v_addc_co_u32_e64 v24, s[4:5], 0, v24, s[22:23]
	v_addc_co_u32_e64 v25, s[4:5], 0, v25, s[24:25]
	v_addc_co_u32_e64 v26, s[4:5], 0, v26, s[26:27]
	v_addc_co_u32_e64 v27, s[4:5], 0, v27, s[28:29]
	v_add_u32_e32 v8, 4, v8
	v_add_u32_e32 v10, 4, v10
	v_add_u32_e32 v12, 4, v12
	v_add_u32_e32 v14, 4, v14
	s_add_i32 s21, s21, 1
	s_branch .Lrs0_loop
.Lrs0_done:
	v_and_b32_e32 v2, 0x1fffff, v17
	v_lshl_add_u32 v28, v24, 2, v28
	v_and_b32_e32 v3, 0x1fffff, v19
	v_lshl_add_u32 v29, v25, 2, v29
	v_and_b32_e32 v4, 0x1fffff, v21
	v_lshl_add_u32 v30, v26, 2, v30
	v_and_b32_e32 v5, 0x1fffff, v23
	v_lshl_add_u32 v31, v27, 2, v31
.Lw1t67:
	s_cbranch_execz .Lw1c67
.Lw1b67:
	s_mov_b64 exec, s[10:11]
	ds_write_b32 v28, v2 offset:32768
	s_mov_b64 exec, s[12:13]
	ds_write_b32 v29, v3 offset:32768
	s_mov_b64 exec, s[14:15]
	ds_write_b32 v30, v4 offset:32768
	s_mov_b64 exec, s[16:17]
	ds_write_b32 v31, v5 offset:32768
	s_mov_b64 exec, -1
.LBB1_332:
	s_cmpk_lt_i32 s3, 0x1001
	s_cbranch_scc1 .LBB1_382
	v_add_u32_e32 v2, 4096, v0
	v_cmp_gt_i32_e64 s[10:11], s3, v2
	ds_read_b32 v17, v1 offset:16384
	v_add_u32_e32 v16, 16384, v1
	v_add_u32_e32 v2, 5120, v0
	v_cmp_gt_i32_e64 s[12:13], s3, v2
	ds_read_b32 v19, v1 offset:20480
	v_add_u32_e32 v18, 20480, v1
.Lw1t68:
	s_cbranch_execz .Lw1c68
.Lw1b68:
	v_add_u32_e32 v2, 6144, v0
	v_cmp_gt_i32_e64 s[14:15], s3, v2
	ds_read_b32 v21, v1 offset:24576
	v_add_u32_e32 v20, 24576, v1
	v_add_u32_e32 v2, 7168, v0
	v_cmp_gt_i32_e64 s[16:17], s3, v2
	ds_read_b32 v23, v1 offset:28672
	v_add_u32_e32 v22, 28672, v1
	s_waitcnt lgkmcnt(0)
	v_lshrrev_b32_e32 v2, 15, v17
	v_and_b32_e32 v2, s19, v2
	v_lshrrev_b32_e32 v3, 15, v19
	v_and_b32_e32 v3, s19, v3
	v_lshrrev_b32_e32 v4, 15, v21
	v_and_b32_e32 v4, s19, v4
	v_lshrrev_b32_e32 v5, 15, v23
	v_and_b32_e32 v5, s19, v5
	v_cndmask_b32_e64 v2, 0, v2, s[10:11]
	v_add_u32_e32 v2, s20, v2
	v_cndmask_b32_e64 v3, 0, v3, s[12:13]
	v_add_u32_e32 v3, s20, v3

.LBB1_384:
	s_or_b64 exec, exec, s[6:7]
	s_sub_i32 s14, s3, s4
	s_ashr_i32 s15, s14, 2
	v_cmp_gt_i32_e32 vcc, s15, v0
	s_and_saveexec_b64 s[6:7], vcc
	s_cbranch_execz .LBB1_387
	s_ashr_i32 s5, s4, 31
	s_lshl_b64 s[10:11], s[4:5], 2
	s_add_u32 s10, s8, s10
	v_lshlrev_b32_e32 v4, 4, v0
	s_addc_u32 s11, s9, s11
	v_mov_b32_e32 v5, 0
	v_lshl_add_u32 v1, s4, 2, v4
.Lw1t74:
	s_cbranch_execz .Lw1c74
.Lw1b74:
	v_lshl_add_u64 v[2:3], s[10:11], 0, v[4:5]
	v_add_u32_e32 v1, 0x8000, v1
	s_mov_b64 s[10:11], 0
	s_mov_b64 s[12:13], 0x4000
	v_mov_b32_e32 v4, v0

.LBB1_387:
	s_or_b64 exec, exec, s[6:7]
	s_and_b32 s6, s14, -4
	s_add_i32 s6, s6, s4
	s_sub_i32 s3, s3, s6
	v_cmp_gt_i32_e32 vcc, s3, v0
.Lw1t75:
	s_cbranch_execz .Lw1c75
.Lw1b75:
	s_and_saveexec_b64 s[4:5], vcc
	s_cbranch_execz .LBB1_389
	v_add_u32_e32 v2, s6, v0
	v_lshlrev_b32_e32 v1, 2, v2
	ds_read_b32 v1, v1 offset:32768
	v_ashrrev_i32_e32 v3, 31, v2
	v_lshl_add_u64 v[2:3], v[2:3], 2, s[8:9]
	s_waitcnt lgkmcnt(0)
	global_store_dword v[2:3], v1, off

.Lmy_cvt1:
	v_cmp_eq_u32_e32 vcc, 0, v4
	s_waitcnt vmcnt(6)
	s_add_i32 s8, s3, 792
	s_lshl_b32 s9, s8, 14
	s_add_u32 s10, s22, s9
	s_addc_u32 s11, s23, 0
	s_mov_b64 exec, s[24:25]
	v_cvt_pk_f16_f32 v8, v8, v9
	v_cvt_pk_f16_f32 v9, v10, v11
	v_cvt_pk_f16_f32 v10, v12, v13
	v_cvt_pk_f16_f32 v11, v14, v15
	v_cndmask_b32_e32 v12, v8, v10, vcc

.Lw1b76:
	v_cndmask_b32_e32 v13, v9, v11, vcc
	s_nop 1
	v_mov_b32_dpp v12, v12 quad_perm:[1,0,3,2] row_mask:0xf bank_mask:0xf bound_ctrl:1
	v_mov_b32_dpp v13, v13 quad_perm:[1,0,3,2] row_mask:0xf bank_mask:0xf bound_ctrl:1
	v_cndmask_b32_e32 v8, v12, v8, vcc
	v_cndmask_b32_e32 v9, v13, v9, vcc
	v_cndmask_b32_e32 v10, v10, v12, vcc
	v_cndmask_b32_e32 v11, v11, v13, vcc
	global_store_dwordx4 v5, v[8:11], s[10:11] sc1
	s_waitcnt vmcnt(5)
	s_add_i32 s8, s3, 985
	s_lshl_b32 s9, s8, 14
	s_add_u32 s10, s22, s9
	s_addc_u32 s11, s23, 0
	s_mov_b64 exec, s[26:27]
	v_cvt_pk_f16_f32 v16, v16, v17
	v_cvt_pk_f16_f32 v17, v18, v19
	v_cvt_pk_f16_f32 v18, v20, v21
	v_cvt_pk_f16_f32 v19, v22, v23
	v_cndmask_b32_e32 v20, v16, v18, vcc
	v_cndmask_b32_e32 v21, v17, v19, vcc
	s_nop 1
	v_mov_b32_dpp v20, v20 quad_perm:[1,0,3,2] row_mask:0xf bank_mask:0xf bound_ctrl:1

.Lw1b77:
	v_mov_b32_dpp v21, v21 quad_perm:[1,0,3,2] row_mask:0xf bank_mask:0xf bound_ctrl:1
	v_cndmask_b32_e32 v16, v20, v16, vcc
	v_cndmask_b32_e32 v17, v21, v17, vcc
	v_cndmask_b32_e32 v18, v18, v20, vcc
	v_cndmask_b32_e32 v19, v19, v21, vcc
	global_store_dwordx4 v5, v[16:19], s[10:11] sc1
	s_waitcnt vmcnt(4)
	s_add_i32 s8, s3, 1178
	s_lshl_b32 s9, s8, 14
	s_add_u32 s10, s22, s9
	s_addc_u32 s11, s23, 0
	s_mov_b64 exec, s[28:29]
	v_cvt_pk_f16_f32 v24, v24, v25
	v_cvt_pk_f16_f32 v25, v26, v27
	v_cvt_pk_f16_f32 v26, v28, v29
	v_cvt_pk_f16_f32 v27, v30, v31
	v_cndmask_b32_e32 v28, v24, v26, vcc
	v_cndmask_b32_e32 v29, v25, v27, vcc
	s_nop 1
	v_mov_b32_dpp v28, v28 quad_perm:[1,0,3,2] row_mask:0xf bank_mask:0xf bound_ctrl:1
	v_mov_b32_dpp v29, v29 quad_perm:[1,0,3,2] row_mask:0xf bank_mask:0xf bound_ctrl:1

.Lw1b78:
	v_cndmask_b32_e32 v24, v28, v24, vcc
	v_cndmask_b32_e32 v25, v29, v25, vcc
	v_cndmask_b32_e32 v26, v26, v28, vcc
	v_cndmask_b32_e32 v27, v27, v29, vcc
	global_store_dwordx4 v5, v[24:27], s[10:11] sc1
	s_waitcnt vmcnt(3)
	s_add_i32 s8, s3, 1371
	s_lshl_b32 s9, s8, 14
	s_add_u32 s10, s22, s9
	s_addc_u32 s11, s23, 0
	s_mov_b64 exec, s[30:31]
	v_cvt_pk_f16_f32 v32, v32, v33
	v_cvt_pk_f16_f32 v33, v34, v35
	v_cvt_pk_f16_f32 v34, v36, v37
	v_cvt_pk_f16_f32 v35, v38, v39
	v_cndmask_b32_e32 v36, v32, v34, vcc
	v_cndmask_b32_e32 v37, v33, v35, vcc
	s_nop 1
	v_mov_b32_dpp v36, v36 quad_perm:[1,0,3,2] row_mask:0xf bank_mask:0xf bound_ctrl:1
	v_mov_b32_dpp v37, v37 quad_perm:[1,0,3,2] row_mask:0xf bank_mask:0xf bound_ctrl:1
	v_cndmask_b32_e32 v32, v36, v32, vcc
	v_cndmask_b32_e32 v33, v37, v33, vcc
	v_cndmask_b32_e32 v34, v34, v36, vcc

.Lw1b79:
	v_cndmask_b32_e32 v35, v35, v37, vcc
	global_store_dwordx4 v5, v[32:35], s[10:11] sc1
